# v69 variant: converting workgroups run the rope-k tiles (6,7) in round 0 and rope-q (4,5) in round 1
# speedup vs baseline: 1.0146x; 1.0097x over previous
;     __device__ bool next(int i, Unit& u) const { if (!base.next(i >> 1, u)) return false; if (i & 1) { u.pm += MTOK / BM; u.pn += DM / BM; } return true; }
;   __device__ __forceinline__ bool next(int i,AttnUnit&u)const{ if(i>=2||vcu>=256)return false; const int s=vcu&3; u.bh=vcu>>2; u.qb=(i==0)?7-s:s; return true; }
;     __host__ __device__ bool next(int i, Unit& u) const {
;         const int L = i * G + c; if (L >= nwg) return false;
;         int wgid = L; { const int q = nwg / NXCD, r = nwg % NXCD, xcd = wgid % NXCD, off = wgid / NXCD; wgid = (xcd < r ? xcd * (q + 1) : r * (q + 1) + (xcd - r) * q) + off; }
;         const int nig = WGM * nN, gid = wgid / nig, fm = gid * WGM, gsz = (nM - fm) < WGM ? (nM - fm) : WGM;
;         u.pm = fm + ((wgid % nig) % gsz); u.pn = (wgid % nig) / gsz; u.half = 0; return true;
.LBB0_382:
	s_ashr_i32 s4, s21, 31
	s_lshr_b32 s4, s4, 29
	s_add_i32 s4, s21, s4
	s_ashr_i32 s5, s4, 3
	s_and_b32 s4, s4, -8
	s_sub_i32 s4, s21, s4
	s_cmp_lt_i32 s4, 0
	s_movk_i32 s6, 0x91
	s_cselect_b32 s6, s6, 0x90
	s_mul_i32 s4, s4, s6
	s_add_i32 s4, s4, s5
	s_mul_hi_i32 s5, s4, 0x38e38e39
	s_lshr_b32 s6, s5, 31
	s_ashr_i32 s5, s5, 5
	s_add_i32 s5, s5, s6
	s_lshl_b32 s6, s5, 3
	s_mulk_i32 s5, 0x90
	s_sub_i32 s4, s4, s5
	s_bfe_u32 s5, s4, 0x3001c
	s_add_i32 s5, s4, s5
	s_sext_i32_i16 s7, s5
	s_and_b32 s5, s5, 0xfff8
	s_sub_i32 s4, s4, s5
	s_sext_i32_i16 s4, s4
	s_add_i32 s18, s6, s4
	s_ashr_i32 s70, s7, 3
	s_mul_i32 s4, s70, 5
	s_cmp_lt_u32 s70, 12
	s_cbranch_scc0 .Lpn_hi0
	s_mov_b32 s6, 0x6239820
	s_mov_b32 s7, 0x5a92829
	s_branch .Lpn_go0

;     __device__ bool next(int i, Unit& u) const { if (!base.next(i >> 1, u)) return false; if (i & 1) { u.pm += MTOK / BM; u.pn += DM / BM; } return true; }
;   __device__ __forceinline__ bool next(int i,AttnUnit&u)const{ if(i>=2||vcu>=256)return false; const int s=vcu&3; u.bh=vcu>>2; u.qb=(i==0)?7-s:s; return true; }
;     __host__ __device__ bool next(int i, Unit& u) const {
;         const int L = i * G + c; if (L >= nwg) return false;
;         int wgid = L; { const int q = nwg / NXCD, r = nwg % NXCD, xcd = wgid % NXCD, off = wgid / NXCD; wgid = (xcd < r ? xcd * (q + 1) : r * (q + 1) + (xcd - r) * q) + off; }
;         const int nig = WGM * nN, gid = wgid / nig, fm = gid * WGM, gsz = (nM - fm) < WGM ? (nM - fm) : WGM;
;         u.pm = fm + ((wgid % nig) % gsz); u.pn = (wgid % nig) / gsz; u.half = 0; return true;
; template <class Epi, class Sched, bool ALIGN_EPI = false, bool SP2 = false>
; __device__ __forceinline__ void gemm_phase(PG8_LAS unsigned char* lds, const Gemm g, const Sched& S, const Epi& E) {
;     ...
;         const bool has_next = S.next(ui + 1, nxt);
;         const char* nA = has_next ? (const char*)g.A + (size_t)nxt.pm * tstep + (nxt.half == 2 ? hstep : (size_t)0) : cA; const char* nB = has_next ? (const char*)g.Bt + (size_t)nxt.pn * tstep : cB;
.LBB0_392:
	s_add_i32 s72, s72, 1
	s_mul_i32 s10, s72, s33
	s_add_i32 s10, s10, s21
	s_cmpk_lt_i32 s10, 0x480
	s_cselect_b64 s[64:65], -1, 0
	s_cmpk_gt_i32 s10, 0x47f
	s_cbranch_scc1 .LBB0_394
	s_ashr_i32 s11, s10, 31
	s_lshr_b32 s11, s11, 29
	s_add_i32 s11, s10, s11
	s_ashr_i32 s12, s11, 3
	s_and_b32 s11, s11, -8
	s_sub_i32 s10, s10, s11
	s_cmp_lt_i32 s10, 0
	s_movk_i32 s11, 0x91
	s_cselect_b32 s11, s11, 0x90
	s_mul_i32 s10, s10, s11
	s_add_i32 s10, s10, s12
	s_mul_hi_i32 s11, s10, 0x38e38e39
	s_lshr_b32 s12, s11, 31
	s_ashr_i32 s11, s11, 5
	s_add_i32 s11, s11, s12
	s_lshl_b32 s12, s11, 3
	s_mulk_i32 s11, 0x90
	s_sub_i32 s10, s10, s11
	s_bfe_u32 s11, s10, 0x3001c
	s_add_i32 s11, s10, s11
	s_sext_i32_i16 s13, s11
	s_and_b32 s11, s11, 0xfff8
	s_sub_i32 s10, s10, s11
	s_sext_i32_i16 s10, s10
	s_add_i32 s60, s12, s10
	s_ashr_i32 s62, s13, 3
	s_mul_i32 s10, s62, 5
	s_cmp_lt_u32 s62, 12
	s_cbranch_scc0 .Lpn_hi1
	s_mov_b32 s12, 0x6239820
	s_mov_b32 s13, 0x5a92829
	s_branch .Lpn_go1
